# br1: res1 + branch-merge epilogue requests both halves' gate rows up front
# speedup vs baseline: 1.0113x; 1.0030x over previous
; __device__ __forceinline__ unsigned cvt_pk_bf16(float lo, float hi) { unsigned r; asm volatile("v_cvt_pk_bf16_f32 %0, %1, %2" : "=v"(r) : "v"(lo), "v"(hi)); return r; }
; __device__ __forceinline__ float bf_lo(unsigned w) { return __uint_as_float(w << 16); }
; __device__ __forceinline__ float bf_hi(unsigned w) { return __uint_as_float(w & 0xffff0000u); }
; __device__ __forceinline__ void st16_wt(void* p, u32x4 w) { asm volatile("global_store_dwordx4 %0, %1, off sc1\n\ts_nop 1" :: "v"(p), "v"(w) : "memory"); }
;     __device__ __forceinline__ bool operator()(f32x4 (&acc)[2][2][4][2], const pg8::Unit& u, int wr, int wc, int fr, int fq) const {
;         const int row0 = u.pm * 256 + wr * 64 + fr, colb = u.pn * 256 + wc * 32 + 8 * fq; const bool first = (u.aux == 0);
;         const bf16_t* gp = G + (first ? 0 : 1024);
; #pragma unroll
;         for (int ai = 0; ai < 2; ++ai) {
;             u32x4 gin[4][2];
; #pragma unroll
;             for (int m = 0; m < 4; ++m)
; #pragma unroll
;                 for (int bj = 0; bj < 2; ++bj) gin[m][bj] = *(const u32x4*)(gp + (size_t)(row0 + ai * 128 + m * 16) * 2048 + colb + bj * 128);
; #pragma unroll
;             for (int m = 0; m < 4; ++m) { const int row = row0 + ai * 128 + m * 16;
; #pragma unroll
;                 for (int bj = 0; bj < 2; ++bj) { const u32x4 g = gin[m][bj];
;                     const f32x4 f0 = {bf_lo(g.x), bf_hi(g.x), bf_lo(g.y), bf_hi(g.y)}, f1 = {bf_lo(g.z), bf_hi(g.z), bf_lo(g.w), bf_hi(g.w)};
;                     if (first) { acc[ai][bj][m][0] *= f0; acc[ai][bj][m][1] *= f1; }
;                     else { const f32x4 v0 = acc[ai][bj][m][0] * f0, v1 = acc[ai][bj][m][1] * f1; u32x4 w; w.x = cvt_pk_bf16(v0[0], v0[1]); w.y = cvt_pk_bf16(v0[2], v0[3]); w.z = cvt_pk_bf16(v1[0], v1[1]); w.w = cvt_pk_bf16(v1[2], v1[3]);
;                         st16_wt(Mo + (size_t)row * DM + colb + bj * 128, w); } } } }
.LBB0_936:
	s_cmp_lg_u32 s33, 0
	s_cselect_b64 s[20:21], -1, 0
	s_cmp_eq_u32 s33, 0
	s_cselect_b64 s[2:3], -1, 0
	s_and_b64 vcc, s[2:3], exec
	s_cselect_b32 s2, 0, 0x800
	v_readlane_b32 s8, v251, 50
	v_lshl_add_u32 v166, s36, 8, v198
	v_lshl_or_b32 v180, s39, 8, v200
	v_readlane_b32 s9, v251, 51
	s_add_u32 s2, s8, s2
	s_addc_u32 s3, s9, 0
	v_ashrrev_i32_e32 v181, 31, v180
	v_ashrrev_i32_e32 v167, 31, v166
	v_lshl_add_u64 v[182:183], v[180:181], 1, s[2:3]
	v_lshlrev_b64 v[56:57], 12, v[166:167]
	v_or_b32_e32 v188, 16, v166
	v_lshl_add_u64 v[60:61], v[182:183], 0, v[56:57]
	v_ashrrev_i32_e32 v189, 31, v188
	global_load_dwordx4 v[56:59], v[60:61], off
	global_load_dwordx4 v[84:87], v[60:61], off offset:256
	v_lshlrev_b64 v[60:61], 12, v[188:189]
	v_or_b32_e32 v186, 32, v166
	v_lshl_add_u64 v[60:61], v[182:183], 0, v[60:61]
	v_ashrrev_i32_e32 v187, 31, v186
	global_load_dwordx4 v[80:83], v[60:61], off
	global_load_dwordx4 v[116:119], v[60:61], off offset:256
	v_lshlrev_b64 v[60:61], 12, v[186:187]
	v_or_b32_e32 v184, 48, v166
	v_lshl_add_u64 v[60:61], v[182:183], 0, v[60:61]
	v_ashrrev_i32_e32 v185, 31, v184
	global_load_dwordx4 v[112:115], v[60:61], off
	global_load_dwordx4 v[140:143], v[60:61], off offset:256
	v_lshlrev_b64 v[60:61], 12, v[184:185]
	v_lshl_add_u64 v[60:61], v[182:183], 0, v[60:61]
	global_load_dwordx4 v[136:139], v[60:61], off
	global_load_dwordx4 v[162:165], v[60:61], off offset:256
	v_add_u32_e32 v202, 0x80, v166
	v_lshlrev_b32_e32 v202, 12, v202
	v_mov_b32_e32 v203, 0
	v_lshl_add_u64 v[214:215], v[182:183], 0, v[202:203]
	global_load_dwordx4 v[204:207], v[214:215], off
	global_load_dwordx4 v[208:211], v[214:215], off offset:256
	v_add_u32_e32 v202, 0x10000, v202
	v_lshl_add_u64 v[214:215], v[182:183], 0, v[202:203]
	global_load_dwordx4 v[216:219], v[214:215], off
	global_load_dwordx4 v[220:223], v[214:215], off offset:256
	v_add_u32_e32 v202, 0x10000, v202
	v_lshl_add_u64 v[214:215], v[182:183], 0, v[202:203]
	global_load_dwordx4 v[224:227], v[214:215], off
	global_load_dwordx4 v[232:235], v[214:215], off offset:256
	v_add_u32_e32 v202, 0x10000, v202
	v_lshl_add_u64 v[214:215], v[182:183], 0, v[202:203]
	global_load_dwordx4 v[240:243], v[214:215], off
	global_load_dwordx4 v[244:247], v[214:215], off offset:256
	v_readlane_b32 s2, v252, 4
	v_lshlrev_b64 v[60:61], 11, v[166:167]
	v_readlane_b32 s3, v252, 5
	s_waitcnt vmcnt(0)
	v_lshlrev_b32_e32 v190, 16, v58
	v_lshl_add_u64 v[60:61], s[2:3], 0, v[60:61]
	v_lshl_add_u64 v[196:197], v[180:181], 1, v[60:61]
	v_lshlrev_b32_e32 v60, 16, v56
	v_and_b32_e32 v61, 0xffff0000, v56
	v_lshlrev_b32_e32 v56, 16, v57
	v_and_b32_e32 v57, 0xffff0000, v57
	v_and_b32_e32 v191, 0xffff0000, v58
	v_lshlrev_b32_e32 v58, 16, v59
	v_and_b32_e32 v59, 0xffff0000, v59
	v_pk_mul_f32 v[62:63], v[78:79], v[56:57]
	v_pk_mul_f32 v[60:61], v[76:77], v[60:61]
	v_pk_mul_f32 v[58:59], v[74:75], v[58:59]
	v_pk_mul_f32 v[56:57], v[72:73], v[190:191]
	s_cbranch_vccnz .LBB0_938
	v_cvt_pk_bf16_f32 v60, v60, v61
	v_cvt_pk_bf16_f32 v61, v62, v63
	v_cvt_pk_bf16_f32 v62, v56, v57
	v_cvt_pk_bf16_f32 v63, v58, v59
	v_mov_b64_e32 v[56:57], v[72:73]
	global_store_dwordx4 v[196:197], v[60:63], off sc1
	s_nop 1
	v_mov_b64_e32 v[60:61], v[76:77]
	v_mov_b64_e32 v[58:59], v[74:75]
	v_mov_b64_e32 v[62:63], v[78:79]

; __device__ __forceinline__ unsigned cvt_pk_bf16(float lo, float hi) { unsigned r; asm volatile("v_cvt_pk_bf16_f32 %0, %1, %2" : "=v"(r) : "v"(lo), "v"(hi)); return r; }
; __device__ __forceinline__ float bf_lo(unsigned w) { return __uint_as_float(w << 16); }
; __device__ __forceinline__ float bf_hi(unsigned w) { return __uint_as_float(w & 0xffff0000u); }
; __device__ __forceinline__ void st16_wt(void* p, u32x4 w) { asm volatile("global_store_dwordx4 %0, %1, off sc1\n\ts_nop 1" :: "v"(p), "v"(w) : "memory"); }
;     __device__ __forceinline__ bool operator()(f32x4 (&acc)[2][2][4][2], const pg8::Unit& u, int wr, int wc, int fr, int fq) const {
;     ...
;             for (int m = 0; m < 4; ++m)
; #pragma unroll
;                 for (int bj = 0; bj < 2; ++bj) gin[m][bj] = *(const u32x4*)(gp + (size_t)(row0 + ai * 128 + m * 16) * 2048 + colb + bj * 128);
; #pragma unroll
;             for (int m = 0; m < 4; ++m) { const int row = row0 + ai * 128 + m * 16;
; #pragma unroll
;                 for (int bj = 0; bj < 2; ++bj) { const u32x4 g = gin[m][bj];
;                     const f32x4 f0 = {bf_lo(g.x), bf_hi(g.x), bf_lo(g.y), bf_hi(g.y)}, f1 = {bf_lo(g.z), bf_hi(g.z), bf_lo(g.w), bf_hi(g.w)};
;                     if (first) { acc[ai][bj][m][0] *= f0; acc[ai][bj][m][1] *= f1; }
;                     else { const f32x4 v0 = acc[ai][bj][m][0] * f0, v1 = acc[ai][bj][m][1] * f1; u32x4 w; w.x = cvt_pk_bf16(v0[0], v0[1]); w.y = cvt_pk_bf16(v0[2], v0[3]); w.z = cvt_pk_bf16(v1[0], v1[1]); w.w = cvt_pk_bf16(v1[2], v1[3]);
;                         st16_wt(Mo + (size_t)row * DM + colb + bj * 128, w); } } } }
.LBB0_952:
	v_add_u32_e32 v92, 0x80, v166
	v_ashrrev_i32_e32 v93, 31, v92
	v_lshlrev_b64 v[88:89], 12, v[92:93]
	v_add_u32_e32 v186, 0x90, v166
	v_lshl_add_u64 v[94:95], v[182:183], 0, v[88:89]
	v_ashrrev_i32_e32 v187, 31, v186
	v_lshlrev_b64 v[94:95], 12, v[186:187]
	v_add_u32_e32 v184, 0xa0, v166
	v_lshl_add_u64 v[94:95], v[182:183], 0, v[94:95]
	v_ashrrev_i32_e32 v185, 31, v184
	v_lshlrev_b64 v[94:95], 12, v[184:185]
	v_add_u32_e32 v166, 0xb0, v166
	v_lshl_add_u64 v[94:95], v[182:183], 0, v[94:95]
	v_ashrrev_i32_e32 v167, 31, v166
	v_lshlrev_b64 v[94:95], 12, v[166:167]
	v_lshl_add_u64 v[94:95], v[182:183], 0, v[94:95]
	v_lshlrev_b64 v[92:93], 11, v[92:93]
	v_lshl_add_u64 v[182:183], s[2:3], 0, v[92:93]
	s_and_b64 vcc, exec, s[12:13]
	v_lshl_add_u64 v[182:183], v[180:181], 1, v[182:183]
	v_lshlrev_b32_e32 v92, 16, v204
	v_and_b32_e32 v93, 0xffff0000, v204
	v_lshlrev_b32_e32 v88, 16, v205
	v_and_b32_e32 v89, 0xffff0000, v205
	v_lshlrev_b32_e32 v188, 16, v206
	v_and_b32_e32 v189, 0xffff0000, v206
	v_lshlrev_b32_e32 v90, 16, v207
	v_and_b32_e32 v91, 0xffff0000, v207
	v_pk_mul_f32 v[94:95], v[70:71], v[88:89]
	v_pk_mul_f32 v[92:93], v[68:69], v[92:93]
	v_pk_mul_f32 v[90:91], v[66:67], v[90:91]
	v_pk_mul_f32 v[88:89], v[64:65], v[188:189]
	s_cbranch_vccnz .LBB0_954
	v_cvt_pk_bf16_f32 v92, v92, v93
	v_cvt_pk_bf16_f32 v93, v94, v95
	v_cvt_pk_bf16_f32 v94, v88, v89
	v_cvt_pk_bf16_f32 v95, v90, v91
	v_mov_b64_e32 v[90:91], v[66:67]
	global_store_dwordx4 v[182:183], v[92:95], off sc1
	s_nop 1
	v_mov_b64_e32 v[94:95], v[70:71]
	v_mov_b64_e32 v[88:89], v[64:65]
	v_mov_b64_e32 v[92:93], v[68:69]
.LBB0_954:
	v_lshlrev_b32_e32 v64, 16, v208
	v_and_b32_e32 v65, 0xffff0000, v208
	v_lshlrev_b32_e32 v66, 16, v209
	v_and_b32_e32 v67, 0xffff0000, v209
	v_lshlrev_b32_e32 v68, 16, v210
	v_and_b32_e32 v69, 0xffff0000, v210
	v_lshlrev_b32_e32 v70, 16, v211
	v_and_b32_e32 v71, 0xffff0000, v211
	v_pk_mul_f32 v[66:67], v[54:55], v[66:67]
	v_pk_mul_f32 v[64:65], v[52:53], v[64:65]
	v_pk_mul_f32 v[70:71], v[50:51], v[70:71]
	s_and_b64 vcc, exec, s[12:13]
	v_pk_mul_f32 v[68:69], v[48:49], v[68:69]
	s_cbranch_vccnz .LBB0_956
	s_mov_b64 s[8:9], 0x100
	v_cvt_pk_bf16_f32 v64, v64, v65
	v_cvt_pk_bf16_f32 v65, v66, v67
	v_cvt_pk_bf16_f32 v66, v68, v69
	v_cvt_pk_bf16_f32 v67, v70, v71
	v_lshl_add_u64 v[68:69], v[182:183], 0, s[8:9]
	global_store_dwordx4 v[68:69], v[64:67], off sc1
	s_nop 1
	v_mov_b64_e32 v[70:71], v[50:51]
	v_mov_b64_e32 v[66:67], v[54:55]
	v_mov_b64_e32 v[68:69], v[48:49]
	v_mov_b64_e32 v[64:65], v[52:53]
.LBB0_956:
	v_lshlrev_b64 v[48:49], 11, v[186:187]
	v_lshlrev_b32_e32 v50, 16, v216
	v_and_b32_e32 v51, 0xffff0000, v216
	v_lshlrev_b32_e32 v52, 16, v217
	v_and_b32_e32 v53, 0xffff0000, v217
	v_lshlrev_b32_e32 v54, 16, v218
	v_and_b32_e32 v55, 0xffff0000, v218
	v_lshlrev_b32_e32 v124, 16, v219
	v_and_b32_e32 v125, 0xffff0000, v219
	v_lshl_add_u64 v[48:49], s[2:3], 0, v[48:49]
	v_pk_mul_f32 v[122:123], v[46:47], v[52:53]
	v_pk_mul_f32 v[120:121], v[44:45], v[50:51]
	v_pk_mul_f32 v[126:127], v[42:43], v[124:125]
	v_pk_mul_f32 v[124:125], v[40:41], v[54:55]
	s_and_b64 vcc, exec, s[12:13]
	v_lshl_add_u64 v[48:49], v[180:181], 1, v[48:49]
	s_cbranch_vccnz .LBB0_958
	v_cvt_pk_bf16_f32 v50, v120, v121
	v_cvt_pk_bf16_f32 v51, v122, v123
	v_cvt_pk_bf16_f32 v52, v124, v125
	v_cvt_pk_bf16_f32 v53, v126, v127
	v_mov_b64_e32 v[126:127], v[42:43]
	global_store_dwordx4 v[48:49], v[50:53], off sc1
	s_nop 1
	v_mov_b64_e32 v[122:123], v[46:47]
	v_mov_b64_e32 v[124:125], v[40:41]
	v_mov_b64_e32 v[120:121], v[44:45]
; __device__ __forceinline__ unsigned cvt_pk_bf16(float lo, float hi) { unsigned r; asm volatile("v_cvt_pk_bf16_f32 %0, %1, %2" : "=v"(r) : "v"(lo), "v"(hi)); return r; }
; __device__ __forceinline__ float bf_lo(unsigned w) { return __uint_as_float(w << 16); }
; __device__ __forceinline__ float bf_hi(unsigned w) { return __uint_as_float(w & 0xffff0000u); }
; __device__ __forceinline__ void st16_wt(void* p, u32x4 w) { asm volatile("global_store_dwordx4 %0, %1, off sc1\n\ts_nop 1" :: "v"(p), "v"(w) : "memory"); }
;     __device__ __forceinline__ bool operator()(f32x4 (&acc)[2][2][4][2], const pg8::Unit& u, int wr, int wc, int fr, int fq) const {
;     ...
;             for (int m = 0; m < 4; ++m) { const int row = row0 + ai * 128 + m * 16;
; #pragma unroll
;                 for (int bj = 0; bj < 2; ++bj) { const u32x4 g = gin[m][bj];
;                     const f32x4 f0 = {bf_lo(g.x), bf_hi(g.x), bf_lo(g.y), bf_hi(g.y)}, f1 = {bf_lo(g.z), bf_hi(g.z), bf_lo(g.w), bf_hi(g.w)};
;                     if (first) { acc[ai][bj][m][0] *= f0; acc[ai][bj][m][1] *= f1; }
;                     else { const f32x4 v0 = acc[ai][bj][m][0] * f0, v1 = acc[ai][bj][m][1] * f1; u32x4 w; w.x = cvt_pk_bf16(v0[0], v0[1]); w.y = cvt_pk_bf16(v0[2], v0[3]); w.z = cvt_pk_bf16(v1[0], v1[1]); w.w = cvt_pk_bf16(v1[2], v1[3]);
;                         st16_wt(Mo + (size_t)row * DM + colb + bj * 128, w); } } } }
.LBB0_958:
	v_lshlrev_b32_e32 v40, 16, v220
	v_and_b32_e32 v41, 0xffff0000, v220
	v_lshlrev_b32_e32 v42, 16, v221
	v_and_b32_e32 v43, 0xffff0000, v221
	v_lshlrev_b32_e32 v44, 16, v222
	v_and_b32_e32 v45, 0xffff0000, v222
	v_lshlrev_b32_e32 v46, 16, v223
	v_and_b32_e32 v47, 0xffff0000, v223
	v_pk_mul_f32 v[42:43], v[38:39], v[42:43]
	v_pk_mul_f32 v[40:41], v[36:37], v[40:41]
	v_pk_mul_f32 v[46:47], v[34:35], v[46:47]
	s_and_b64 vcc, exec, s[12:13]
	v_pk_mul_f32 v[44:45], v[32:33], v[44:45]
	s_cbranch_vccnz .LBB0_960
	s_mov_b64 s[8:9], 0x100
	v_cvt_pk_bf16_f32 v40, v40, v41
	v_cvt_pk_bf16_f32 v41, v42, v43
	v_cvt_pk_bf16_f32 v42, v44, v45
	v_cvt_pk_bf16_f32 v43, v46, v47
	v_lshl_add_u64 v[44:45], v[48:49], 0, s[8:9]
	global_store_dwordx4 v[44:45], v[40:43], off sc1
	s_nop 1
	v_mov_b64_e32 v[46:47], v[34:35]
	v_mov_b64_e32 v[42:43], v[38:39]
	v_mov_b64_e32 v[44:45], v[32:33]
	v_mov_b64_e32 v[40:41], v[36:37]
.LBB0_960:
	v_lshlrev_b64 v[32:33], 11, v[184:185]
	v_lshlrev_b32_e32 v34, 16, v224
	v_and_b32_e32 v35, 0xffff0000, v224
	v_lshlrev_b32_e32 v36, 16, v225
	v_and_b32_e32 v37, 0xffff0000, v225
	v_lshlrev_b32_e32 v38, 16, v226
	v_and_b32_e32 v39, 0xffff0000, v226
	v_lshlrev_b32_e32 v48, 16, v227
	v_and_b32_e32 v49, 0xffff0000, v227
	v_lshl_add_u64 v[32:33], s[2:3], 0, v[32:33]
	v_pk_mul_f32 v[146:147], v[30:31], v[36:37]
	v_pk_mul_f32 v[144:145], v[28:29], v[34:35]
	v_pk_mul_f32 v[150:151], v[26:27], v[48:49]
	v_pk_mul_f32 v[148:149], v[24:25], v[38:39]
	s_and_b64 vcc, exec, s[12:13]
	v_lshl_add_u64 v[32:33], v[180:181], 1, v[32:33]
	s_cbranch_vccnz .LBB0_962
	v_cvt_pk_bf16_f32 v34, v144, v145
	v_cvt_pk_bf16_f32 v35, v146, v147
	v_cvt_pk_bf16_f32 v36, v148, v149
	v_cvt_pk_bf16_f32 v37, v150, v151
	v_mov_b64_e32 v[150:151], v[26:27]
	global_store_dwordx4 v[32:33], v[34:37], off sc1
	s_nop 1
	v_mov_b64_e32 v[146:147], v[30:31]
	v_mov_b64_e32 v[148:149], v[24:25]
	v_mov_b64_e32 v[144:145], v[28:29]
.LBB0_962:
	v_lshlrev_b32_e32 v24, 16, v232
	v_and_b32_e32 v25, 0xffff0000, v232
	v_lshlrev_b32_e32 v26, 16, v233
	v_and_b32_e32 v27, 0xffff0000, v233
	v_lshlrev_b32_e32 v28, 16, v234
	v_and_b32_e32 v29, 0xffff0000, v234
	v_lshlrev_b32_e32 v30, 16, v235
	v_and_b32_e32 v31, 0xffff0000, v235
	v_pk_mul_f32 v[26:27], v[22:23], v[26:27]
	v_pk_mul_f32 v[24:25], v[20:21], v[24:25]
	v_pk_mul_f32 v[30:31], v[18:19], v[30:31]
	s_and_b64 vcc, exec, s[12:13]
	v_pk_mul_f32 v[28:29], v[16:17], v[28:29]
	s_cbranch_vccnz .LBB0_964
	s_mov_b64 s[8:9], 0x100
	v_cvt_pk_bf16_f32 v24, v24, v25
	v_cvt_pk_bf16_f32 v25, v26, v27
	v_cvt_pk_bf16_f32 v26, v28, v29
	v_cvt_pk_bf16_f32 v27, v30, v31
	v_lshl_add_u64 v[28:29], v[32:33], 0, s[8:9]
	global_store_dwordx4 v[28:29], v[24:27], off sc1
	s_nop 1
	v_mov_b64_e32 v[30:31], v[18:19]
	v_mov_b64_e32 v[26:27], v[22:23]
	v_mov_b64_e32 v[28:29], v[16:17]
	v_mov_b64_e32 v[24:25], v[20:21]
.LBB0_964:
	v_lshlrev_b64 v[16:17], 11, v[166:167]
	v_lshlrev_b32_e32 v18, 16, v240
	v_and_b32_e32 v19, 0xffff0000, v240
	v_lshlrev_b32_e32 v20, 16, v241
	v_and_b32_e32 v21, 0xffff0000, v241
	v_lshlrev_b32_e32 v22, 16, v242
	v_and_b32_e32 v23, 0xffff0000, v242
	v_lshlrev_b32_e32 v32, 16, v243
	v_and_b32_e32 v33, 0xffff0000, v243
	v_lshl_add_u64 v[16:17], s[2:3], 0, v[16:17]
	v_pk_mul_f32 v[158:159], v[14:15], v[20:21]
	v_pk_mul_f32 v[156:157], v[12:13], v[18:19]
	v_pk_mul_f32 v[166:167], v[10:11], v[32:33]
	v_pk_mul_f32 v[164:165], v[8:9], v[22:23]
	s_and_b64 vcc, exec, s[12:13]
	v_lshl_add_u64 v[16:17], v[180:181], 1, v[16:17]
	s_cbranch_vccnz .LBB0_966
	v_cvt_pk_bf16_f32 v18, v156, v157
	v_cvt_pk_bf16_f32 v19, v158, v159
	v_cvt_pk_bf16_f32 v20, v164, v165
	v_cvt_pk_bf16_f32 v21, v166, v167
	v_mov_b64_e32 v[166:167], v[10:11]
	global_store_dwordx4 v[16:17], v[18:21], off sc1
	s_nop 1
	v_mov_b64_e32 v[158:159], v[14:15]
	v_mov_b64_e32 v[164:165], v[8:9]
	v_mov_b64_e32 v[156:157], v[12:13]
.LBB0_966:
	v_lshlrev_b32_e32 v8, 16, v244
	v_and_b32_e32 v9, 0xffff0000, v244
	v_lshlrev_b32_e32 v10, 16, v245
	v_and_b32_e32 v11, 0xffff0000, v245
	v_lshlrev_b32_e32 v12, 16, v246
	v_and_b32_e32 v13, 0xffff0000, v246
	v_lshlrev_b32_e32 v14, 16, v247
	v_and_b32_e32 v15, 0xffff0000, v247
	v_pk_mul_f32 v[10:11], v[6:7], v[10:11]
	v_pk_mul_f32 v[8:9], v[4:5], v[8:9]
	v_pk_mul_f32 v[14:15], v[2:3], v[14:15]
	s_and_b64 vcc, exec, s[12:13]
	v_pk_mul_f32 v[12:13], v[0:1], v[12:13]
	s_cbranch_vccz .LBB0_969
	s_and_b64 vcc, exec, s[12:13]
	s_cbranch_vccz .LBB0_970
